# in-proj-0 conversion workgroups: hand-written routine with three rotating load buffers (two items in flight)
# speedup vs baseline: 1.0119x; 1.0068x over previous
.Lp2c0_loop:
	s_add_i32 s7, s4, s5
	s_add_i32 s29, s7, s5
	s_cmp_lt_u32 s29, s6
	s_cbranch_scc0 .Lp2c0_A_n2
	s_lshr_b32 s22, s29, 8
	s_and_b32 s23, s29, 0xff
	s_and_b32 s27, s22, 1
	s_lshr_b32 s22, s22, 1
	s_cmp_eq_u32 s27, 0
	s_cselect_b64 s[16:17], s[12:13], s[14:15]
	s_add_i32 s22, s22, 20
	s_lshl_b32 s24, s22, 22
	s_lshr_b32 s25, s23, 5
	s_lshl_b32 s25, s25, 19
	s_and_b32 s26, s23, 31
	s_lshl_b32 s26, s26, 7
	s_add_i32 s24, s24, s25
	s_add_i32 s24, s24, s26
	s_add_u32 s16, s16, s24
	s_addc_u32 s17, s17, 0
	s_nop 0
	global_load_dwordx4 v[160:163], v136, s[16:17] nt
	global_load_dwordx4 v[164:167], v137, s[16:17] nt
	global_load_dwordx4 v[168:171], v138, s[16:17] nt
	global_load_dwordx4 v[172:175], v139, s[16:17] nt
	s_add_u32 s16, s16, 0x4000
	s_addc_u32 s17, s17, 0
	s_nop 0
	global_load_dwordx4 v[176:179], v136, s[16:17] nt
	global_load_dwordx4 v[180:183], v137, s[16:17] nt
	global_load_dwordx4 v[184:187], v138, s[16:17] nt
	global_load_dwordx4 v[188:191], v139, s[16:17] nt
	s_add_u32 s16, s16, 0x4000
	s_addc_u32 s17, s17, 0
	s_nop 0
	global_load_dwordx4 v[192:195], v136, s[16:17] nt
	global_load_dwordx4 v[196:199], v137, s[16:17] nt
	global_load_dwordx4 v[200:203], v138, s[16:17] nt
	global_load_dwordx4 v[204:207], v139, s[16:17] nt
	s_add_u32 s16, s16, 0x4000
	s_addc_u32 s17, s17, 0
	s_nop 0
	global_load_dwordx4 v[208:211], v136, s[16:17] nt
	global_load_dwordx4 v[212:215], v137, s[16:17] nt
	global_load_dwordx4 v[216:219], v138, s[16:17] nt
	global_load_dwordx4 v[220:223], v139, s[16:17] nt
	s_waitcnt vmcnt(32)
	s_branch .Lp2c0_A_st
.Lp2c0_A_n2:
	s_cmp_lt_u32 s7, s6
	s_cbranch_scc0 .Lp2c0_A_n1
	s_waitcnt vmcnt(16)
	s_branch .Lp2c0_A_st

.Lp2c0_A_st:
	s_lshr_b32 s22, s4, 8
	s_and_b32 s23, s4, 0xff
	s_and_b32 s27, s22, 1
	s_lshr_b32 s22, s22, 1
	s_add_i32 s22, s22, 20
	s_mul_i32 s24, s22, 0x300000
	s_lshr_b32 s25, s23, 5
	s_lshl_b32 s25, s25, 7
	s_add_i32 s24, s24, s25
	s_and_b32 s26, s23, 31
	s_lshr_b32 s25, s26, 2
	s_lshl_b32 s25, s25, 18
	s_add_i32 s24, s24, s25
	s_lshl_b32 s25, s27, 17
	s_add_i32 s24, s24, s25
	s_and_b32 s25, s26, 3
	s_lshl_b32 s25, s25, 15
	s_add_i32 s24, s24, s25
	s_add_u32 s20, s10, s24
	s_addc_u32 s21, s11, 0
	v_mul_f32_e32 v0, 0x42000000, v0
	v_mul_f32_e32 v4, 0x42000000, v4
	v_mul_f32_e32 v8, 0x42000000, v8
	v_mul_f32_e32 v12, 0x42000000, v12
	v_mul_f32_e32 v16, 0x42000000, v16
	v_mul_f32_e32 v20, 0x42000000, v20
	v_mul_f32_e32 v24, 0x42000000, v24
	v_mul_f32_e32 v28, 0x42000000, v28
	v_mul_f32_e32 v32, 0x42000000, v32
	v_mul_f32_e32 v36, 0x42000000, v36
	v_mul_f32_e32 v40, 0x42000000, v40
	v_mul_f32_e32 v44, 0x42000000, v44
	v_mul_f32_e32 v48, 0x42000000, v48
	v_mul_f32_e32 v52, 0x42000000, v52
	v_mul_f32_e32 v56, 0x42000000, v56
	v_mul_f32_e32 v60, 0x42000000, v60
	v_med3_f32 v0, v0, s28, v141
	v_med3_f32 v4, v4, s28, v141
	v_med3_f32 v8, v8, s28, v141
	v_med3_f32 v12, v12, s28, v141
	v_med3_f32 v16, v16, s28, v141
	v_med3_f32 v20, v20, s28, v141
	v_med3_f32 v24, v24, s28, v141
	v_med3_f32 v28, v28, s28, v141
	v_med3_f32 v32, v32, s28, v141
	v_med3_f32 v36, v36, s28, v141
	v_med3_f32 v40, v40, s28, v141
	v_med3_f32 v44, v44, s28, v141
	v_med3_f32 v48, v48, s28, v141
	v_med3_f32 v52, v52, s28, v141
	v_med3_f32 v56, v56, s28, v141
	v_med3_f32 v60, v60, s28, v141
	v_cvt_pk_fp8_f32 v128, v0, v4
	v_cvt_pk_fp8_f32 v129, v16, v20
	v_cvt_pk_fp8_f32 v130, v32, v36
	v_cvt_pk_fp8_f32 v131, v48, v52
	v_cvt_pk_fp8_f32 v128, v8, v12 op_sel:[0,0,1]
	v_cvt_pk_fp8_f32 v129, v24, v28 op_sel:[0,0,1]
	v_cvt_pk_fp8_f32 v130, v40, v44 op_sel:[0,0,1]
	v_cvt_pk_fp8_f32 v131, v56, v60 op_sel:[0,0,1]
	s_nop 0
	global_store_dwordx4 v140, v[128:131], s[20:21]
	v_mul_f32_e32 v1, 0x42000000, v1
	v_mul_f32_e32 v5, 0x42000000, v5
	v_mul_f32_e32 v9, 0x42000000, v9
	v_mul_f32_e32 v13, 0x42000000, v13
	v_mul_f32_e32 v17, 0x42000000, v17
	v_mul_f32_e32 v21, 0x42000000, v21
	v_mul_f32_e32 v25, 0x42000000, v25
	v_mul_f32_e32 v29, 0x42000000, v29
	v_mul_f32_e32 v33, 0x42000000, v33
	v_mul_f32_e32 v37, 0x42000000, v37
	v_mul_f32_e32 v41, 0x42000000, v41
	v_mul_f32_e32 v45, 0x42000000, v45
	v_mul_f32_e32 v49, 0x42000000, v49
	v_mul_f32_e32 v53, 0x42000000, v53
	v_mul_f32_e32 v57, 0x42000000, v57
	v_mul_f32_e32 v61, 0x42000000, v61
	v_med3_f32 v1, v1, s28, v141
	v_med3_f32 v5, v5, s28, v141
	v_med3_f32 v9, v9, s28, v141
	v_med3_f32 v13, v13, s28, v141
	v_med3_f32 v17, v17, s28, v141
	v_med3_f32 v21, v21, s28, v141
	v_med3_f32 v25, v25, s28, v141
	v_med3_f32 v29, v29, s28, v141
	v_med3_f32 v33, v33, s28, v141
	v_med3_f32 v37, v37, s28, v141
	v_med3_f32 v41, v41, s28, v141
	v_med3_f32 v45, v45, s28, v141
	v_med3_f32 v49, v49, s28, v141
	v_med3_f32 v53, v53, s28, v141
	v_med3_f32 v57, v57, s28, v141
	v_med3_f32 v61, v61, s28, v141
	v_cvt_pk_fp8_f32 v132, v1, v5
	v_cvt_pk_fp8_f32 v133, v17, v21
	v_cvt_pk_fp8_f32 v134, v33, v37
	v_cvt_pk_fp8_f32 v135, v49, v53
	v_cvt_pk_fp8_f32 v132, v9, v13 op_sel:[0,0,1]
	v_cvt_pk_fp8_f32 v133, v25, v29 op_sel:[0,0,1]
	v_cvt_pk_fp8_f32 v134, v41, v45 op_sel:[0,0,1]
	v_cvt_pk_fp8_f32 v135, v57, v61 op_sel:[0,0,1]
	s_nop 0
	global_store_dwordx4 v140, v[132:135], s[20:21] offset:1024
	v_mul_f32_e32 v2, 0x42000000, v2
	v_mul_f32_e32 v6, 0x42000000, v6
	v_mul_f32_e32 v10, 0x42000000, v10
	v_mul_f32_e32 v14, 0x42000000, v14
	v_mul_f32_e32 v18, 0x42000000, v18
	v_mul_f32_e32 v22, 0x42000000, v22
	v_mul_f32_e32 v26, 0x42000000, v26
	v_mul_f32_e32 v30, 0x42000000, v30
	v_mul_f32_e32 v34, 0x42000000, v34
	v_mul_f32_e32 v38, 0x42000000, v38
	v_mul_f32_e32 v42, 0x42000000, v42
	v_mul_f32_e32 v46, 0x42000000, v46
	v_mul_f32_e32 v50, 0x42000000, v50
	v_mul_f32_e32 v54, 0x42000000, v54
	v_mul_f32_e32 v58, 0x42000000, v58
	v_mul_f32_e32 v62, 0x42000000, v62
	v_med3_f32 v2, v2, s28, v141
	v_med3_f32 v6, v6, s28, v141
	v_med3_f32 v10, v10, s28, v141
	v_med3_f32 v14, v14, s28, v141
	v_med3_f32 v18, v18, s28, v141
	v_med3_f32 v22, v22, s28, v141
	v_med3_f32 v26, v26, s28, v141
	v_med3_f32 v30, v30, s28, v141
	v_med3_f32 v34, v34, s28, v141
	v_med3_f32 v38, v38, s28, v141
	v_med3_f32 v42, v42, s28, v141
	v_med3_f32 v46, v46, s28, v141
	v_med3_f32 v50, v50, s28, v141
	v_med3_f32 v54, v54, s28, v141
	v_med3_f32 v58, v58, s28, v141
	v_med3_f32 v62, v62, s28, v141
	v_cvt_pk_fp8_f32 v128, v2, v6
	v_cvt_pk_fp8_f32 v129, v18, v22
	v_cvt_pk_fp8_f32 v130, v34, v38
	v_cvt_pk_fp8_f32 v131, v50, v54
	v_cvt_pk_fp8_f32 v128, v10, v14 op_sel:[0,0,1]
	v_cvt_pk_fp8_f32 v129, v26, v30 op_sel:[0,0,1]
	v_cvt_pk_fp8_f32 v130, v42, v46 op_sel:[0,0,1]
	v_cvt_pk_fp8_f32 v131, v58, v62 op_sel:[0,0,1]
	s_nop 0
	global_store_dwordx4 v140, v[128:131], s[20:21] offset:2048
	v_mul_f32_e32 v3, 0x42000000, v3
	v_mul_f32_e32 v7, 0x42000000, v7
	v_mul_f32_e32 v11, 0x42000000, v11
	v_mul_f32_e32 v15, 0x42000000, v15
	v_mul_f32_e32 v19, 0x42000000, v19
	v_mul_f32_e32 v23, 0x42000000, v23
	v_mul_f32_e32 v27, 0x42000000, v27
	v_mul_f32_e32 v31, 0x42000000, v31
	v_mul_f32_e32 v35, 0x42000000, v35
	v_mul_f32_e32 v39, 0x42000000, v39
	v_mul_f32_e32 v43, 0x42000000, v43
	v_mul_f32_e32 v47, 0x42000000, v47
	v_mul_f32_e32 v51, 0x42000000, v51
	v_mul_f32_e32 v55, 0x42000000, v55
	v_mul_f32_e32 v59, 0x42000000, v59
	v_mul_f32_e32 v63, 0x42000000, v63
	v_med3_f32 v3, v3, s28, v141
	v_med3_f32 v7, v7, s28, v141
	v_med3_f32 v11, v11, s28, v141
	v_med3_f32 v15, v15, s28, v141
	v_med3_f32 v19, v19, s28, v141
	v_med3_f32 v23, v23, s28, v141
	v_med3_f32 v27, v27, s28, v141
	v_med3_f32 v31, v31, s28, v141
	v_med3_f32 v35, v35, s28, v141
	v_med3_f32 v39, v39, s28, v141
	v_med3_f32 v43, v43, s28, v141
	v_med3_f32 v47, v47, s28, v141
	v_med3_f32 v51, v51, s28, v141
	v_med3_f32 v55, v55, s28, v141
	v_med3_f32 v59, v59, s28, v141
	v_med3_f32 v63, v63, s28, v141
	v_cvt_pk_fp8_f32 v132, v3, v7
	v_cvt_pk_fp8_f32 v133, v19, v23
	v_cvt_pk_fp8_f32 v134, v35, v39
	v_cvt_pk_fp8_f32 v135, v51, v55
	v_cvt_pk_fp8_f32 v132, v11, v15 op_sel:[0,0,1]
	v_cvt_pk_fp8_f32 v133, v27, v31 op_sel:[0,0,1]
	v_cvt_pk_fp8_f32 v134, v43, v47 op_sel:[0,0,1]
	v_cvt_pk_fp8_f32 v135, v59, v63 op_sel:[0,0,1]
	s_nop 0
	global_store_dwordx4 v140, v[132:135], s[20:21] offset:3072
	s_cmp_ge_u32 s7, s6
	s_cbranch_scc1 .Lp2c0_done
	s_mov_b32 s4, s7
	s_add_i32 s7, s4, s5
	s_add_i32 s29, s7, s5
	s_cmp_lt_u32 s29, s6
	s_cbranch_scc0 .Lp2c0_B_n2
	s_lshr_b32 s22, s29, 8
	s_and_b32 s23, s29, 0xff
	s_and_b32 s27, s22, 1
	s_lshr_b32 s22, s22, 1
	s_cmp_eq_u32 s27, 0
	s_cselect_b64 s[16:17], s[12:13], s[14:15]
	s_add_i32 s22, s22, 20
	s_lshl_b32 s24, s22, 22
	s_lshr_b32 s25, s23, 5
	s_lshl_b32 s25, s25, 19
	s_and_b32 s26, s23, 31
	s_lshl_b32 s26, s26, 7
	s_add_i32 s24, s24, s25
	s_add_i32 s24, s24, s26
	s_add_u32 s16, s16, s24
	s_addc_u32 s17, s17, 0
	s_nop 0
	global_load_dwordx4 v[0:3], v136, s[16:17] nt
	global_load_dwordx4 v[4:7], v137, s[16:17] nt
	global_load_dwordx4 v[8:11], v138, s[16:17] nt
	global_load_dwordx4 v[12:15], v139, s[16:17] nt
	s_add_u32 s16, s16, 0x4000
	s_addc_u32 s17, s17, 0
	s_nop 0
	global_load_dwordx4 v[16:19], v136, s[16:17] nt
	global_load_dwordx4 v[20:23], v137, s[16:17] nt
	global_load_dwordx4 v[24:27], v138, s[16:17] nt
	global_load_dwordx4 v[28:31], v139, s[16:17] nt
	s_add_u32 s16, s16, 0x4000
	s_addc_u32 s17, s17, 0
	s_nop 0
	global_load_dwordx4 v[32:35], v136, s[16:17] nt
	global_load_dwordx4 v[36:39], v137, s[16:17] nt
	global_load_dwordx4 v[40:43], v138, s[16:17] nt
	global_load_dwordx4 v[44:47], v139, s[16:17] nt
	s_add_u32 s16, s16, 0x4000
	s_addc_u32 s17, s17, 0
	s_nop 0
	global_load_dwordx4 v[48:51], v136, s[16:17] nt
	global_load_dwordx4 v[52:55], v137, s[16:17] nt
	global_load_dwordx4 v[56:59], v138, s[16:17] nt
	global_load_dwordx4 v[60:63], v139, s[16:17] nt
	s_waitcnt vmcnt(32)
	s_branch .Lp2c0_B_st

.Lp2c0_B_st:
	s_lshr_b32 s22, s4, 8
	s_and_b32 s23, s4, 0xff
	s_and_b32 s27, s22, 1
	s_lshr_b32 s22, s22, 1
	s_add_i32 s22, s22, 20
	s_mul_i32 s24, s22, 0x300000
	s_lshr_b32 s25, s23, 5
	s_lshl_b32 s25, s25, 7
	s_add_i32 s24, s24, s25
	s_and_b32 s26, s23, 31
	s_lshr_b32 s25, s26, 2
	s_lshl_b32 s25, s25, 18
	s_add_i32 s24, s24, s25
	s_lshl_b32 s25, s27, 17
	s_add_i32 s24, s24, s25
	s_and_b32 s25, s26, 3
	s_lshl_b32 s25, s25, 15
	s_add_i32 s24, s24, s25
	s_add_u32 s20, s10, s24
	s_addc_u32 s21, s11, 0
	v_mul_f32_e32 v64, 0x42000000, v64
	v_mul_f32_e32 v68, 0x42000000, v68
	v_mul_f32_e32 v72, 0x42000000, v72
	v_mul_f32_e32 v76, 0x42000000, v76
	v_mul_f32_e32 v80, 0x42000000, v80
	v_mul_f32_e32 v84, 0x42000000, v84
	v_mul_f32_e32 v88, 0x42000000, v88
	v_mul_f32_e32 v92, 0x42000000, v92
	v_mul_f32_e32 v96, 0x42000000, v96
	v_mul_f32_e32 v100, 0x42000000, v100
	v_mul_f32_e32 v104, 0x42000000, v104
	v_mul_f32_e32 v108, 0x42000000, v108
	v_mul_f32_e32 v112, 0x42000000, v112
	v_mul_f32_e32 v116, 0x42000000, v116
	v_mul_f32_e32 v120, 0x42000000, v120
	v_mul_f32_e32 v124, 0x42000000, v124
	v_med3_f32 v64, v64, s28, v141
	v_med3_f32 v68, v68, s28, v141
	v_med3_f32 v72, v72, s28, v141
	v_med3_f32 v76, v76, s28, v141
	v_med3_f32 v80, v80, s28, v141
	v_med3_f32 v84, v84, s28, v141
	v_med3_f32 v88, v88, s28, v141
	v_med3_f32 v92, v92, s28, v141
	v_med3_f32 v96, v96, s28, v141
	v_med3_f32 v100, v100, s28, v141
	v_med3_f32 v104, v104, s28, v141
	v_med3_f32 v108, v108, s28, v141
	v_med3_f32 v112, v112, s28, v141
	v_med3_f32 v116, v116, s28, v141
	v_med3_f32 v120, v120, s28, v141
	v_med3_f32 v124, v124, s28, v141
	v_cvt_pk_fp8_f32 v128, v64, v68
	v_cvt_pk_fp8_f32 v129, v80, v84
	v_cvt_pk_fp8_f32 v130, v96, v100
	v_cvt_pk_fp8_f32 v131, v112, v116
	v_cvt_pk_fp8_f32 v128, v72, v76 op_sel:[0,0,1]
	v_cvt_pk_fp8_f32 v129, v88, v92 op_sel:[0,0,1]
	v_cvt_pk_fp8_f32 v130, v104, v108 op_sel:[0,0,1]
	v_cvt_pk_fp8_f32 v131, v120, v124 op_sel:[0,0,1]
	s_nop 0
	global_store_dwordx4 v140, v[128:131], s[20:21]
	v_mul_f32_e32 v65, 0x42000000, v65
	v_mul_f32_e32 v69, 0x42000000, v69
	v_mul_f32_e32 v73, 0x42000000, v73
	v_mul_f32_e32 v77, 0x42000000, v77
	v_mul_f32_e32 v81, 0x42000000, v81
	v_mul_f32_e32 v85, 0x42000000, v85
	v_mul_f32_e32 v89, 0x42000000, v89
	v_mul_f32_e32 v93, 0x42000000, v93
	v_mul_f32_e32 v97, 0x42000000, v97
	v_mul_f32_e32 v101, 0x42000000, v101
	v_mul_f32_e32 v105, 0x42000000, v105
	v_mul_f32_e32 v109, 0x42000000, v109
	v_mul_f32_e32 v113, 0x42000000, v113
	v_mul_f32_e32 v117, 0x42000000, v117
	v_mul_f32_e32 v121, 0x42000000, v121
	v_mul_f32_e32 v125, 0x42000000, v125
	v_med3_f32 v65, v65, s28, v141
	v_med3_f32 v69, v69, s28, v141
	v_med3_f32 v73, v73, s28, v141
	v_med3_f32 v77, v77, s28, v141
	v_med3_f32 v81, v81, s28, v141
	v_med3_f32 v85, v85, s28, v141
	v_med3_f32 v89, v89, s28, v141
	v_med3_f32 v93, v93, s28, v141
	v_med3_f32 v97, v97, s28, v141
	v_med3_f32 v101, v101, s28, v141
	v_med3_f32 v105, v105, s28, v141
	v_med3_f32 v109, v109, s28, v141
	v_med3_f32 v113, v113, s28, v141
	v_med3_f32 v117, v117, s28, v141
	v_med3_f32 v121, v121, s28, v141
	v_med3_f32 v125, v125, s28, v141
	v_cvt_pk_fp8_f32 v132, v65, v69
	v_cvt_pk_fp8_f32 v133, v81, v85
	v_cvt_pk_fp8_f32 v134, v97, v101
	v_cvt_pk_fp8_f32 v135, v113, v117
	v_cvt_pk_fp8_f32 v132, v73, v77 op_sel:[0,0,1]
	v_cvt_pk_fp8_f32 v133, v89, v93 op_sel:[0,0,1]
	v_cvt_pk_fp8_f32 v134, v105, v109 op_sel:[0,0,1]
	v_cvt_pk_fp8_f32 v135, v121, v125 op_sel:[0,0,1]
	s_nop 0
	global_store_dwordx4 v140, v[132:135], s[20:21] offset:1024
	v_mul_f32_e32 v66, 0x42000000, v66
	v_mul_f32_e32 v70, 0x42000000, v70
	v_mul_f32_e32 v74, 0x42000000, v74
	v_mul_f32_e32 v78, 0x42000000, v78
	v_mul_f32_e32 v82, 0x42000000, v82
	v_mul_f32_e32 v86, 0x42000000, v86
	v_mul_f32_e32 v90, 0x42000000, v90
	v_mul_f32_e32 v94, 0x42000000, v94
	v_mul_f32_e32 v98, 0x42000000, v98
	v_mul_f32_e32 v102, 0x42000000, v102
	v_mul_f32_e32 v106, 0x42000000, v106
	v_mul_f32_e32 v110, 0x42000000, v110
	v_mul_f32_e32 v114, 0x42000000, v114
	v_mul_f32_e32 v118, 0x42000000, v118
	v_mul_f32_e32 v122, 0x42000000, v122
	v_mul_f32_e32 v126, 0x42000000, v126
	v_med3_f32 v66, v66, s28, v141
	v_med3_f32 v70, v70, s28, v141
	v_med3_f32 v74, v74, s28, v141
	v_med3_f32 v78, v78, s28, v141
	v_med3_f32 v82, v82, s28, v141
	v_med3_f32 v86, v86, s28, v141
	v_med3_f32 v90, v90, s28, v141
	v_med3_f32 v94, v94, s28, v141
	v_med3_f32 v98, v98, s28, v141
	v_med3_f32 v102, v102, s28, v141
	v_med3_f32 v106, v106, s28, v141
	v_med3_f32 v110, v110, s28, v141
	v_med3_f32 v114, v114, s28, v141
	v_med3_f32 v118, v118, s28, v141
	v_med3_f32 v122, v122, s28, v141
	v_med3_f32 v126, v126, s28, v141
	v_cvt_pk_fp8_f32 v128, v66, v70
	v_cvt_pk_fp8_f32 v129, v82, v86
	v_cvt_pk_fp8_f32 v130, v98, v102
	v_cvt_pk_fp8_f32 v131, v114, v118
	v_cvt_pk_fp8_f32 v128, v74, v78 op_sel:[0,0,1]
	v_cvt_pk_fp8_f32 v129, v90, v94 op_sel:[0,0,1]
	v_cvt_pk_fp8_f32 v130, v106, v110 op_sel:[0,0,1]
	v_cvt_pk_fp8_f32 v131, v122, v126 op_sel:[0,0,1]
	s_nop 0
	global_store_dwordx4 v140, v[128:131], s[20:21] offset:2048
	v_mul_f32_e32 v67, 0x42000000, v67
	v_mul_f32_e32 v71, 0x42000000, v71
	v_mul_f32_e32 v75, 0x42000000, v75
	v_mul_f32_e32 v79, 0x42000000, v79
	v_mul_f32_e32 v83, 0x42000000, v83
	v_mul_f32_e32 v87, 0x42000000, v87
	v_mul_f32_e32 v91, 0x42000000, v91
	v_mul_f32_e32 v95, 0x42000000, v95
	v_mul_f32_e32 v99, 0x42000000, v99
	v_mul_f32_e32 v103, 0x42000000, v103
	v_mul_f32_e32 v107, 0x42000000, v107
	v_mul_f32_e32 v111, 0x42000000, v111
	v_mul_f32_e32 v115, 0x42000000, v115
	v_mul_f32_e32 v119, 0x42000000, v119
	v_mul_f32_e32 v123, 0x42000000, v123
	v_mul_f32_e32 v127, 0x42000000, v127
	v_med3_f32 v67, v67, s28, v141
	v_med3_f32 v71, v71, s28, v141
	v_med3_f32 v75, v75, s28, v141
	v_med3_f32 v79, v79, s28, v141
	v_med3_f32 v83, v83, s28, v141
	v_med3_f32 v87, v87, s28, v141
	v_med3_f32 v91, v91, s28, v141
	v_med3_f32 v95, v95, s28, v141
	v_med3_f32 v99, v99, s28, v141
	v_med3_f32 v103, v103, s28, v141
	v_med3_f32 v107, v107, s28, v141
	v_med3_f32 v111, v111, s28, v141
	v_med3_f32 v115, v115, s28, v141
	v_med3_f32 v119, v119, s28, v141
	v_med3_f32 v123, v123, s28, v141
	v_med3_f32 v127, v127, s28, v141
	v_cvt_pk_fp8_f32 v132, v67, v71
	v_cvt_pk_fp8_f32 v133, v83, v87
	v_cvt_pk_fp8_f32 v134, v99, v103
	v_cvt_pk_fp8_f32 v135, v115, v119
	v_cvt_pk_fp8_f32 v132, v75, v79 op_sel:[0,0,1]
	v_cvt_pk_fp8_f32 v133, v91, v95 op_sel:[0,0,1]
	v_cvt_pk_fp8_f32 v134, v107, v111 op_sel:[0,0,1]
	v_cvt_pk_fp8_f32 v135, v123, v127 op_sel:[0,0,1]
	s_nop 0
	global_store_dwordx4 v140, v[132:135], s[20:21] offset:3072
	s_cmp_ge_u32 s7, s6
	s_cbranch_scc1 .Lp2c0_done
	s_mov_b32 s4, s7
	s_add_i32 s7, s4, s5
	s_add_i32 s29, s7, s5
	s_cmp_lt_u32 s29, s6
	s_cbranch_scc0 .Lp2c0_C_n2
	s_lshr_b32 s22, s29, 8
	s_and_b32 s23, s29, 0xff
	s_and_b32 s27, s22, 1
	s_lshr_b32 s22, s22, 1
	s_cmp_eq_u32 s27, 0
	s_cselect_b64 s[16:17], s[12:13], s[14:15]
	s_add_i32 s22, s22, 20
	s_lshl_b32 s24, s22, 22
	s_lshr_b32 s25, s23, 5
	s_lshl_b32 s25, s25, 19
	s_and_b32 s26, s23, 31
	s_lshl_b32 s26, s26, 7
	s_add_i32 s24, s24, s25
	s_add_i32 s24, s24, s26
	s_add_u32 s16, s16, s24
	s_addc_u32 s17, s17, 0
	s_nop 0
	global_load_dwordx4 v[64:67], v136, s[16:17] nt
	global_load_dwordx4 v[68:71], v137, s[16:17] nt
	global_load_dwordx4 v[72:75], v138, s[16:17] nt
	global_load_dwordx4 v[76:79], v139, s[16:17] nt
	s_add_u32 s16, s16, 0x4000
	s_addc_u32 s17, s17, 0
	s_nop 0
	global_load_dwordx4 v[80:83], v136, s[16:17] nt
	global_load_dwordx4 v[84:87], v137, s[16:17] nt
	global_load_dwordx4 v[88:91], v138, s[16:17] nt
	global_load_dwordx4 v[92:95], v139, s[16:17] nt
	s_add_u32 s16, s16, 0x4000
	s_addc_u32 s17, s17, 0
	s_nop 0
	global_load_dwordx4 v[96:99], v136, s[16:17] nt
	global_load_dwordx4 v[100:103], v137, s[16:17] nt
	global_load_dwordx4 v[104:107], v138, s[16:17] nt
	global_load_dwordx4 v[108:111], v139, s[16:17] nt
	s_add_u32 s16, s16, 0x4000
	s_addc_u32 s17, s17, 0
	s_nop 0
	global_load_dwordx4 v[112:115], v136, s[16:17] nt
	global_load_dwordx4 v[116:119], v137, s[16:17] nt
	global_load_dwordx4 v[120:123], v138, s[16:17] nt
	global_load_dwordx4 v[124:127], v139, s[16:17] nt
	s_waitcnt vmcnt(32)
	s_branch .Lp2c0_C_st

.Lp2c0_C_st:
	s_lshr_b32 s22, s4, 8
	s_and_b32 s23, s4, 0xff
	s_and_b32 s27, s22, 1
	s_lshr_b32 s22, s22, 1
	s_add_i32 s22, s22, 20
	s_mul_i32 s24, s22, 0x300000
	s_lshr_b32 s25, s23, 5
	s_lshl_b32 s25, s25, 7
	s_add_i32 s24, s24, s25
	s_and_b32 s26, s23, 31
	s_lshr_b32 s25, s26, 2
	s_lshl_b32 s25, s25, 18
	s_add_i32 s24, s24, s25
	s_lshl_b32 s25, s27, 17
	s_add_i32 s24, s24, s25
	s_and_b32 s25, s26, 3
	s_lshl_b32 s25, s25, 15
	s_add_i32 s24, s24, s25
	s_add_u32 s20, s10, s24
	s_addc_u32 s21, s11, 0
	v_mul_f32_e32 v160, 0x42000000, v160
	v_mul_f32_e32 v164, 0x42000000, v164
	v_mul_f32_e32 v168, 0x42000000, v168
	v_mul_f32_e32 v172, 0x42000000, v172
	v_mul_f32_e32 v176, 0x42000000, v176
	v_mul_f32_e32 v180, 0x42000000, v180
	v_mul_f32_e32 v184, 0x42000000, v184
	v_mul_f32_e32 v188, 0x42000000, v188
	v_mul_f32_e32 v192, 0x42000000, v192
	v_mul_f32_e32 v196, 0x42000000, v196
	v_mul_f32_e32 v200, 0x42000000, v200
	v_mul_f32_e32 v204, 0x42000000, v204
	v_mul_f32_e32 v208, 0x42000000, v208
	v_mul_f32_e32 v212, 0x42000000, v212
	v_mul_f32_e32 v216, 0x42000000, v216
	v_mul_f32_e32 v220, 0x42000000, v220
	v_med3_f32 v160, v160, s28, v141
	v_med3_f32 v164, v164, s28, v141
	v_med3_f32 v168, v168, s28, v141
	v_med3_f32 v172, v172, s28, v141
	v_med3_f32 v176, v176, s28, v141
	v_med3_f32 v180, v180, s28, v141
	v_med3_f32 v184, v184, s28, v141
	v_med3_f32 v188, v188, s28, v141
	v_med3_f32 v192, v192, s28, v141
	v_med3_f32 v196, v196, s28, v141
	v_med3_f32 v200, v200, s28, v141
	v_med3_f32 v204, v204, s28, v141
	v_med3_f32 v208, v208, s28, v141
	v_med3_f32 v212, v212, s28, v141
	v_med3_f32 v216, v216, s28, v141
	v_med3_f32 v220, v220, s28, v141
	v_cvt_pk_fp8_f32 v128, v160, v164
	v_cvt_pk_fp8_f32 v129, v176, v180
	v_cvt_pk_fp8_f32 v130, v192, v196
	v_cvt_pk_fp8_f32 v131, v208, v212
	v_cvt_pk_fp8_f32 v128, v168, v172 op_sel:[0,0,1]
	v_cvt_pk_fp8_f32 v129, v184, v188 op_sel:[0,0,1]
	v_cvt_pk_fp8_f32 v130, v200, v204 op_sel:[0,0,1]
	v_cvt_pk_fp8_f32 v131, v216, v220 op_sel:[0,0,1]
	s_nop 0
	global_store_dwordx4 v140, v[128:131], s[20:21]
	v_mul_f32_e32 v161, 0x42000000, v161
	v_mul_f32_e32 v165, 0x42000000, v165
	v_mul_f32_e32 v169, 0x42000000, v169
	v_mul_f32_e32 v173, 0x42000000, v173
	v_mul_f32_e32 v177, 0x42000000, v177
	v_mul_f32_e32 v181, 0x42000000, v181
	v_mul_f32_e32 v185, 0x42000000, v185
	v_mul_f32_e32 v189, 0x42000000, v189
	v_mul_f32_e32 v193, 0x42000000, v193
	v_mul_f32_e32 v197, 0x42000000, v197
	v_mul_f32_e32 v201, 0x42000000, v201
	v_mul_f32_e32 v205, 0x42000000, v205
	v_mul_f32_e32 v209, 0x42000000, v209
	v_mul_f32_e32 v213, 0x42000000, v213
	v_mul_f32_e32 v217, 0x42000000, v217
	v_mul_f32_e32 v221, 0x42000000, v221
	v_med3_f32 v161, v161, s28, v141
	v_med3_f32 v165, v165, s28, v141
	v_med3_f32 v169, v169, s28, v141
	v_med3_f32 v173, v173, s28, v141
	v_med3_f32 v177, v177, s28, v141
	v_med3_f32 v181, v181, s28, v141
	v_med3_f32 v185, v185, s28, v141
	v_med3_f32 v189, v189, s28, v141
	v_med3_f32 v193, v193, s28, v141
	v_med3_f32 v197, v197, s28, v141
	v_med3_f32 v201, v201, s28, v141
	v_med3_f32 v205, v205, s28, v141
	v_med3_f32 v209, v209, s28, v141
	v_med3_f32 v213, v213, s28, v141
	v_med3_f32 v217, v217, s28, v141
	v_med3_f32 v221, v221, s28, v141
	v_cvt_pk_fp8_f32 v132, v161, v165
	v_cvt_pk_fp8_f32 v133, v177, v181
	v_cvt_pk_fp8_f32 v134, v193, v197
	v_cvt_pk_fp8_f32 v135, v209, v213
	v_cvt_pk_fp8_f32 v132, v169, v173 op_sel:[0,0,1]
	v_cvt_pk_fp8_f32 v133, v185, v189 op_sel:[0,0,1]
	v_cvt_pk_fp8_f32 v134, v201, v205 op_sel:[0,0,1]
	v_cvt_pk_fp8_f32 v135, v217, v221 op_sel:[0,0,1]
	s_nop 0
	global_store_dwordx4 v140, v[132:135], s[20:21] offset:1024
	v_mul_f32_e32 v162, 0x42000000, v162
	v_mul_f32_e32 v166, 0x42000000, v166
	v_mul_f32_e32 v170, 0x42000000, v170
	v_mul_f32_e32 v174, 0x42000000, v174
	v_mul_f32_e32 v178, 0x42000000, v178
	v_mul_f32_e32 v182, 0x42000000, v182
	v_mul_f32_e32 v186, 0x42000000, v186
	v_mul_f32_e32 v190, 0x42000000, v190
	v_mul_f32_e32 v194, 0x42000000, v194
	v_mul_f32_e32 v198, 0x42000000, v198
	v_mul_f32_e32 v202, 0x42000000, v202
	v_mul_f32_e32 v206, 0x42000000, v206
	v_mul_f32_e32 v210, 0x42000000, v210
	v_mul_f32_e32 v214, 0x42000000, v214
	v_mul_f32_e32 v218, 0x42000000, v218
	v_mul_f32_e32 v222, 0x42000000, v222
	v_med3_f32 v162, v162, s28, v141
	v_med3_f32 v166, v166, s28, v141
	v_med3_f32 v170, v170, s28, v141
	v_med3_f32 v174, v174, s28, v141
	v_med3_f32 v178, v178, s28, v141
	v_med3_f32 v182, v182, s28, v141
	v_med3_f32 v186, v186, s28, v141
	v_med3_f32 v190, v190, s28, v141
	v_med3_f32 v194, v194, s28, v141
	v_med3_f32 v198, v198, s28, v141
	v_med3_f32 v202, v202, s28, v141
	v_med3_f32 v206, v206, s28, v141
	v_med3_f32 v210, v210, s28, v141
	v_med3_f32 v214, v214, s28, v141
	v_med3_f32 v218, v218, s28, v141
	v_med3_f32 v222, v222, s28, v141
	v_cvt_pk_fp8_f32 v128, v162, v166
	v_cvt_pk_fp8_f32 v129, v178, v182
	v_cvt_pk_fp8_f32 v130, v194, v198
	v_cvt_pk_fp8_f32 v131, v210, v214
	v_cvt_pk_fp8_f32 v128, v170, v174 op_sel:[0,0,1]
	v_cvt_pk_fp8_f32 v129, v186, v190 op_sel:[0,0,1]
	v_cvt_pk_fp8_f32 v130, v202, v206 op_sel:[0,0,1]
	v_cvt_pk_fp8_f32 v131, v218, v222 op_sel:[0,0,1]
	s_nop 0
	global_store_dwordx4 v140, v[128:131], s[20:21] offset:2048
	v_mul_f32_e32 v163, 0x42000000, v163
	v_mul_f32_e32 v167, 0x42000000, v167
	v_mul_f32_e32 v171, 0x42000000, v171
	v_mul_f32_e32 v175, 0x42000000, v175
	v_mul_f32_e32 v179, 0x42000000, v179
	v_mul_f32_e32 v183, 0x42000000, v183
	v_mul_f32_e32 v187, 0x42000000, v187
	v_mul_f32_e32 v191, 0x42000000, v191
	v_mul_f32_e32 v195, 0x42000000, v195
	v_mul_f32_e32 v199, 0x42000000, v199
	v_mul_f32_e32 v203, 0x42000000, v203
	v_mul_f32_e32 v207, 0x42000000, v207
	v_mul_f32_e32 v211, 0x42000000, v211
	v_mul_f32_e32 v215, 0x42000000, v215
	v_mul_f32_e32 v219, 0x42000000, v219
	v_mul_f32_e32 v223, 0x42000000, v223
	v_med3_f32 v163, v163, s28, v141
	v_med3_f32 v167, v167, s28, v141
	v_med3_f32 v171, v171, s28, v141
	v_med3_f32 v175, v175, s28, v141
	v_med3_f32 v179, v179, s28, v141
	v_med3_f32 v183, v183, s28, v141
	v_med3_f32 v187, v187, s28, v141
	v_med3_f32 v191, v191, s28, v141
	v_med3_f32 v195, v195, s28, v141
	v_med3_f32 v199, v199, s28, v141
	v_med3_f32 v203, v203, s28, v141
	v_med3_f32 v207, v207, s28, v141
	v_med3_f32 v211, v211, s28, v141
	v_med3_f32 v215, v215, s28, v141
	v_med3_f32 v219, v219, s28, v141
	v_med3_f32 v223, v223, s28, v141
	v_cvt_pk_fp8_f32 v132, v163, v167
	v_cvt_pk_fp8_f32 v133, v179, v183
	v_cvt_pk_fp8_f32 v134, v195, v199
	v_cvt_pk_fp8_f32 v135, v211, v215
	v_cvt_pk_fp8_f32 v132, v171, v175 op_sel:[0,0,1]
	v_cvt_pk_fp8_f32 v133, v187, v191 op_sel:[0,0,1]
	v_cvt_pk_fp8_f32 v134, v203, v207 op_sel:[0,0,1]
	v_cvt_pk_fp8_f32 v135, v219, v223 op_sel:[0,0,1]
	s_nop 0
	global_store_dwordx4 v140, v[132:135], s[20:21] offset:3072
	s_cmp_ge_u32 s7, s6
	s_cbranch_scc1 .Lp2c0_done
	s_mov_b32 s4, s7
	s_branch .Lp2c0_loop
